# LN1: lane i handles columns 8i..8i+7 and 512+8i..: every 16-byte load/store instruction covers 1 KiB contiguous across the wave (was 32-byte stride)
# speedup vs baseline: 1.0267x; 1.0004x over previous
; #define LAS __attribute__((address_space(3)))
; __device__ __forceinline__ void ln1_row(const u32x4 ra, const u32x4 rb, const LAS float* cv  , bf16_t* __restrict__ hf, unsigned char* __restrict__ hf8, float* __restrict__ stats, int row, int lane) {
;     asm volatile("" : "+v"(cv));
;     const int c0 = lane * 16;
;     f32x4 v[4]; float s = 0.f;
;     unpack_t16r(ra, rb, v);
; #pragma unroll
;     for (int j = 0; j < 4; ++j) s += (v[j].x + v[j].y) + (v[j].z + v[j].w);
;     const float mean = wave_sum(s) * (1.f / D); float s2 = 0.f;
; #pragma unroll
;     for (int j = 0; j < 4; ++j) { v[j] = v[j] - mean; s2 += (v[j].x * v[j].x + v[j].y * v[j].y) + (v[j].z * v[j].z + v[j].w * v[j].w); }
;     const float rstd = 1.f / sqrtf(wave_sum(s2) * (1.f / D) + LN_EPS);
;     if (lane == 0) *(f32x2*)(stats + 2 * (size_t)row) = (f32x2){mean, rstd};
;     u32x4 ob[2], o8;
; #pragma unroll
;     for (int j = 0; j < 4; ++j) { const int col = c0 + 4 * j;
;         const f32x4 gg = *(const LAS f32x4*)(cv + col), bv = *(const LAS f32x4*)(cv + 1024 + col), sc1 = *(const LAS f32x4*)(cv + 2048 + col), sh = *(const LAS f32x4*)(cv + 3072 + col);
;         const f32x4 h4 = (v[j] * rstd * gg + bv) * sc1 + sh;
;         const unsigned p0 = pk2(h4.x, h4.y), p1 = pk2(h4.z, h4.w);
;         if (j == 0) { ob[0].x = p0; ob[0].y = p1; } else if (j == 1) { ob[0].z = p0; ob[0].w = p1; } else if (j == 2) { ob[1].x = p0; ob[1].y = p1; } else { ob[1].z = p0; ob[1].w = p1; }
;         const f32x4 h8 = h4 * S_HF8;
;         int w0 = __builtin_amdgcn_cvt_pk_fp8_f32(clamp8(h8.x), clamp8(h8.y), 0, false); w0 = __builtin_amdgcn_cvt_pk_fp8_f32(clamp8(h8.z), clamp8(h8.w), w0, true);
;         if (j == 0) o8.x = (unsigned)w0; else if (j == 1) o8.y = (unsigned)w0; else if (j == 2) o8.z = (unsigned)w0; else o8.w = (unsigned)w0; }
;     *(u32x4*)(hf + (size_t)row * D + c0) = ob[0]; *(u32x4*)(hf + (size_t)row * D + c0 + 8) = ob[1];
;     *(u32x4*)(hf8 + (size_t)row * D + c0) = o8;
; __global__ void __launch_bounds__(NW * 64, 2) mk_fwd(Args args) {
;     ...
;             { const bf16_t* tp = (const bf16_t*)(ws + WS_TB) + (size_t)(c * 256 + wave * 32) * D + lane2 * 16;
;               u32x4 ra = *(const u32x4*)tp, rb = *(const u32x4*)(tp + 8);
; #pragma unroll 1
;               for (int i = 0; i < 32; ++i) {
;                   const u32x4 ca = ra, cb = rb; const int nx = i < 31 ? i + 1 : i;
.LBB0_414:
	s_or_b64 exec, exec, s[4:5]
	s_lshl_b32 s96, s2, 8
	v_readlane_b32 s4, v252, 42
	s_add_i32 s4, s96, s4
	s_ashr_i32 s5, s4, 31
	s_lshl_b64 s[4:5], s[4:5], 11
	v_lshlrev_b32_e32 v16, 4, v0
	s_add_u32 s4, s50, s4
	v_ashrrev_i32_e32 v17, 31, v16
	s_addc_u32 s5, s51, s5
	v_mov_b64_e32 v[2:3], v[16:17]
	v_lshl_add_u64 v[18:19], s[4:5], 0, v[2:3]
	s_waitcnt lgkmcnt(0)
	s_barrier
	v_lshlrev_b32_e32 v122, 1, v16
	ds_read_b128 v[124:127], v122
	ds_read_b128 v[128:131], v122 offset:16
	ds_read_b128 v[132:135], v122 offset:2048
	ds_read_b128 v[136:139], v122 offset:2064
	ds_read_b128 v[140:143], v122 offset:4096
	ds_read_b128 v[144:147], v122 offset:4112
	ds_read_b128 v[148:151], v122 offset:8192
	ds_read_b128 v[152:155], v122 offset:8208
	ds_read_b128 v[156:159], v122 offset:12288
	ds_read_b128 v[162:165], v122 offset:12304
	ds_read_b128 v[166:169], v122 offset:6144
	ds_read_b128 v[170:173], v122 offset:6160
	ds_read_b128 v[174:177], v122 offset:10240
	ds_read_b128 v[178:181], v122 offset:10256
	ds_read_b128 v[182:185], v122 offset:14336
	ds_read_b128 v[186:189], v122 offset:14352
	global_load_dwordx4 v[12:15], v[18:19], off offset:1024
	global_load_dwordx4 v[8:11], v[18:19], off
	v_lshl_add_u64 v[20:21], s[48:49], 0, v[2:3]
	v_lshrrev_b64 v[22:23], 1, v[16:17]
	v_lshl_add_u64 v[22:23], s[58:59], 0, v[22:23]
	v_cmp_ne_u32_e64 s[10:11], 0, v0
	s_movk_i32 s8, 0x400
	s_mov_b32 s6, s1
	global_load_dwordx4 v[114:117], v[18:19], off offset:3072
	global_load_dwordx4 v[118:121], v[18:19], off offset:2048
	s_mov_b32 s99, 0
	s_waitcnt vmcnt(2) lgkmcnt(0)
	s_branch .LBB0_416
.LBB0_415:
	s_or_b64 exec, exec, s[4:5]
	v_mov_b32_e32 v110, v40
	v_mov_b32_e32 v111, v38
	v_mov_b32_e32 v113, v8
	v_mov_b32_e32 v38, v41
	v_pk_mul_f32 v[40:41], v[110:111], v[44:45] op_sel_hi:[1,0]
	v_pk_mul_f32 v[38:39], v[38:39], v[44:45] op_sel_hi:[1,0]
	v_pk_fma_f32 v[40:41], v[40:41], v[124:125], v[140:141]
	v_pk_fma_f32 v[38:39], v[38:39], v[126:127], v[142:143]
	v_pk_fma_f32 v[40:41], v[40:41], v[148:149], v[156:157]
	v_mov_b32_e32 v13, v42
	v_pk_fma_f32 v[42:43], v[38:39], v[150:151], v[158:159]
	v_pk_mul_f32 v[38:39], v[40:41], s[88:89] op_sel_hi:[1,0]
	v_mov_b32_e32 v112, v36
	v_med3_f32 v8, v38, s27, v204
	v_med3_f32 v15, v39, s27, v204
	v_mov_b32_e32 v36, v24
	v_cvt_pk_fp8_f32 v36, v8, v15
	v_pk_mul_f32 v[38:39], v[42:43], s[88:89] op_sel_hi:[1,0]
	v_pk_mul_f32 v[32:33], v[32:33], v[44:45] op_sel_hi:[1,0]
	v_med3_f32 v8, v38, s27, v204
	v_med3_f32 v15, v39, s27, v204
	v_pk_mul_f32 v[38:39], v[112:113], v[44:45] op_sel_hi:[1,0]
	v_cvt_pk_fp8_f32 v36, v8, v15 op_sel:[0,0,1]
	v_pk_fma_f32 v[38:39], v[38:39], v[128:129], v[144:145]
	v_mov_b32_e32 v8, v37
	v_pk_fma_f32 v[46:47], v[38:39], v[152:153], v[162:163]
	v_pk_mul_f32 v[8:9], v[8:9], v[44:45] op_sel_hi:[1,0]
	v_pk_mul_f32 v[38:39], v[46:47], s[88:89] op_sel_hi:[1,0]
	v_mov_b32_e32 v37, v24
	v_med3_f32 v15, v38, s27, v204
	v_med3_f32 v17, v39, s27, v204
	v_pk_fma_f32 v[8:9], v[8:9], v[130:131], v[146:147]
	v_cvt_pk_fp8_f32 v37, v15, v17
	v_pk_fma_f32 v[8:9], v[8:9], v[154:155], v[164:165]
	v_pk_fma_f32 v[32:33], v[32:33], v[132:133], v[166:167]
	v_pk_mul_f32 v[38:39], v[8:9], s[88:89] op_sel_hi:[1,0]
	v_pk_fma_f32 v[32:33], v[32:33], v[174:175], v[182:183]
	v_med3_f32 v15, v38, s27, v204
	v_med3_f32 v17, v39, s27, v204
	v_pk_mul_f32 v[38:39], v[32:33], s[88:89] op_sel_hi:[1,0]
	v_cvt_pk_fp8_f32 v37, v15, v17 op_sel:[0,0,1]
	v_pk_mul_f32 v[34:35], v[34:35], v[44:45] op_sel_hi:[1,0]
	v_med3_f32 v15, v38, s27, v204
	v_med3_f32 v17, v39, s27, v204
	v_mov_b32_e32 v38, v24
	v_pk_fma_f32 v[34:35], v[34:35], v[134:135], v[168:169]
	v_cvt_pk_fp8_f32 v38, v15, v17
	v_pk_fma_f32 v[34:35], v[34:35], v[176:177], v[184:185]
	v_pk_mul_f32 v[12:13], v[12:13], v[44:45] op_sel_hi:[1,0]
	v_pk_mul_f32 v[48:49], v[34:35], s[88:89] op_sel_hi:[1,0]
	v_pk_fma_f32 v[12:13], v[12:13], v[136:137], v[170:171]
	v_med3_f32 v15, v48, s27, v204
	v_med3_f32 v17, v49, s27, v204
	v_cvt_pk_fp8_f32 v38, v15, v17 op_sel:[0,0,1]
	v_mov_b32_e32 v15, v26
	v_pk_mul_f32 v[14:15], v[14:15], v[44:45] op_sel_hi:[1,0]
	v_mov_b32_e32 v39, v24
	v_pk_fma_f32 v[14:15], v[14:15], v[138:139], v[172:173]
	v_pk_fma_f32 v[26:27], v[14:15], v[180:181], v[188:189]
	v_pk_fma_f32 v[14:15], v[12:13], v[178:179], v[186:187]
	v_pk_mul_f32 v[12:13], v[14:15], s[88:89] op_sel_hi:[1,0]
	v_med3_f32 v12, v12, s27, v204
	v_med3_f32 v13, v13, s27, v204
	v_cvt_pk_fp8_f32 v39, v12, v13
	v_pk_mul_f32 v[12:13], v[26:27], s[88:89] op_sel_hi:[1,0]
	v_med3_f32 v12, v12, s27, v204
	v_med3_f32 v13, v13, s27, v204
	v_cvt_pk_fp8_f32 v39, v12, v13 op_sel:[0,0,1]
	v_cvt_pk_bf16_f32 v12, v32, v33
	v_cvt_pk_bf16_f32 v13, v34, v35
	v_cvt_pk_bf16_f32 v14, v14, v15
	v_cvt_pk_bf16_f32 v15, v26, v27
	v_cvt_pk_bf16_f32 v32, v40, v41
	v_cvt_pk_bf16_f32 v33, v42, v43
	v_cvt_pk_bf16_f32 v34, v46, v47
	v_cvt_pk_bf16_f32 v35, v8, v9
	v_lshlrev_b64 v[8:9], 10, v[10:11]
	v_lshlrev_b64 v[10:11], 11, v[10:11]
	v_lshl_add_u64 v[10:11], v[20:21], 0, v[10:11]
	v_lshl_add_u64 v[8:9], v[22:23], 0, v[8:9]
	global_store_dwordx4 v[10:11], v[32:35], off
	global_store_dwordx4 v[10:11], v[12:15], off offset:1024
	global_store_dwordx2 v[8:9], v[36:37], off
	global_store_dwordx2 v[8:9], v[38:39], off offset:512
	s_addk_i32 s8, 0x400
	s_add_i32 s6, s6, 1
	s_waitcnt vmcnt(7)
	s_xor_b32 s99, s99, 1
	s_cbranch_scc0 .Lln1_cpA
	v_mov_b64_e32 v[10:11], v[120:121]
	v_mov_b64_e32 v[14:15], v[116:117]
	v_mov_b64_e32 v[8:9], v[118:119]
	v_mov_b64_e32 v[12:13], v[114:115]
	s_branch .Lln1_cp_done

; __global__ void __launch_bounds__(NW * 64, 2) mk_fwd(Args args) {
;     ...
;               for (int i = 0; i < 32; ++i) {
;                   const u32x4 ca = ra, cb = rb; const int nx = i < 31 ? i + 1 : i;
;                   ra = *(const u32x4*)(tp + (size_t)nx * D); rb = *(const u32x4*)(tp + (size_t)nx * D + 8);
.LBB0_416:
	s_add_i32 s16, s8, 0x400
	s_min_u32 s16, s16, 0x7c00
	v_lshl_add_u64 v[122:123], s[16:17], 1, v[18:19]
	s_cmp_eq_u32 s99, 0
	s_cbranch_scc0 .Lln1_ldB
	global_load_dwordx4 v[0:3], v[122:123], off offset:1024
	global_load_dwordx4 v[4:7], v[122:123], off
	s_branch .Lln1_ld_done
.Lln1_ldB:
	global_load_dwordx4 v[114:117], v[122:123], off offset:1024
	global_load_dwordx4 v[118:121], v[122:123], off
